# out-proj epilogue: the line-contiguous t stores of a block are issued in the next block so the LDS round trip is covered (counted waits re-derived)
# speedup vs baseline: 1.0416x; 1.0048x over previous
; #define LAS __attribute__((address_space(3)))
; __device__ __forceinline__ unsigned cvt_pk_bf16(float lo, float hi) { unsigned r; asm volatile("v_cvt_pk_bf16_f32 %0, %1, %2" : "=v"(r) : "v"(lo), "v"(hi)); return r; }
;     __device__ __forceinline__ void operator()(const f32x4 (&acc)[2][2][4][2], const Unit& u, int wr, int wc, int fr, int fq, const LAS unsigned* rt) const {
;         const int b = (u.pm * BM) >> 11; const int col0 = u.pn * BM + wc * 64 + 16 * fq;
;         f32x4 g[2][2];
; #pragma unroll
;         for (int bj = 0; bj < 2; ++bj)
; #pragma unroll
;             for (int n = 0; n < 2; ++n) g[bj][n] = *(const f32x4*)(mod + b * 6144 + MOD_GATE_A + col0 + 8 * bj + 4 * n) * INV_IN8;
; #pragma unroll
;         for (int ai = 0; ai < 2; ++ai)
; #pragma unroll
;             for (int m = 0; m < 4; ++m) { const size_t o = (size_t)(u.pm * BM + ai * HALF + wr * 64 + m * 16 + fr) * D + col0;
;                 const f32x4 x0 = *(const f32x4*)(x + o), x1 = *(const f32x4*)(x + o + 4), x2 = *(const f32x4*)(x + o + 8), x3 = *(const f32x4*)(x + o + 12);
;                 const f32x4 xs[2][2] = {{x0, x1}, {x2, x3}};
; #pragma unroll
;                 for (int bj = 0; bj < 2; ++bj) {
;                     const f32x4 t0 = xs[bj][0] * ALPHA + g[bj][0] * acc[ai][bj][m][0], t1 = xs[bj][1] * ALPHA + g[bj][1] * acc[ai][bj][m][1];
;                     u32x4 w; w.x = cvt_pk_bf16(t0[0], t0[1]); w.y = cvt_pk_bf16(t0[2], t0[3]); w.z = cvt_pk_bf16(t1[0], t1[1]); w.w = cvt_pk_bf16(t1[2], t1[3]);
;                     *(u32x4*)(tb + o + 8 * bj) = w; } }
.LBB0_409:
	s_lshl_b32 s100, s12, 18
	s_add_i32 s100, s100, s98
	s_bfe_u32 s100, s100, 0x20012
	s_lshr_b32 s4, s65, 3
	s_mulk_i32 s4, 0x1800
	s_ashr_i32 s5, s4, 31
	s_lshl_b64 s[4:5], s[4:5], 2
	v_lshl_add_u32 v16, s100, 8, v185
	s_add_u32 s4, s85, s4
	s_addc_u32 s5, s87, s5
	v_ashrrev_i32_e32 v17, 31, v16
	v_lshl_add_u64 v[0:1], v[16:17], 2, s[4:5]
	s_mov_b64 s[4:5], 0x2000
	v_lshl_add_u64 v[4:5], v[0:1], 0, s[4:5]
	v_add_co_u32_e32 v0, vcc, s41, v0
	s_nop 15
	s_nop 15
	s_nop 1
	v_addc_co_u32_e32 v1, vcc, 0, v1, vcc
	global_load_dwordx4 v[0:3], v[0:1], off
	s_nop 0
	global_load_dwordx4 v[18:21], v[4:5], off offset:48
	global_load_dwordx4 v[174:177], v[4:5], off offset:32
	s_nop 0
	global_load_dwordx4 v[4:7], v[4:5], off offset:16
	s_mov_b64 s[4:5], -1
	s_cmp_eq_u32 s13, 3
	v_lshl_add_u32 v192, s65, 8, v186
	v_ashrrev_i32_e32 v193, 31, v192
	v_lshlrev_b64 v[192:193], 10, v[192:193]
	v_lshl_add_u64 v[192:193], v[192:193], 0, v[16:17]
	v_mbcnt_lo_u32_b32 v26, -1, 0
	v_mbcnt_hi_u32_b32 v26, -1, v26
	v_and_b32_e32 v27, 7, v26
	v_and_b32_e32 v16, 0xffffffc0, v16
	v_lshl_or_b32 v16, v27, 3, v16
	v_lshrrev_b32_e32 v25, 3, v26
	v_mul_u32_u24_e32 v191, 0x90, v25
	v_lshl_add_u32 v191, v27, 4, v191
	v_and_b32_e32 v27, 0xffffffc0, v186
	v_or_b32_e32 v25, v25, v27
	v_lshrrev_b32_e32 v26, 6, v186
	v_lshrrev_b32_e32 v27, 6, v185
	v_lshl_add_u32 v26, v26, 2, v27
	v_mul_u32_u24_e32 v26, 0x900, v26
	v_add_u32_e32 v26, 0x21800, v26
	v_add_u32_e32 v191, v191, v26
	v_and_b32_e32 v27, 15, v186
	v_mul_u32_u24_e32 v190, 0x90, v27
	v_bfe_u32 v27, v185, 4, 2
	v_lshl_add_u32 v190, v27, 5, v190
	v_add_u32_e32 v190, v190, v26
	v_lshl_add_u64 v[250:251], v[192:193], 2, s[18:19]
	s_mov_b32 s101, 0
	global_load_dwordx4 v[206:209], v[250:251], off offset:48
	global_load_dwordx4 v[210:213], v[250:251], off offset:32
	global_load_dwordx4 v[214:217], v[250:251], off offset:16
	global_load_dwordx4 v[218:221], v[250:251], off
	s_mov_b32 s100, 0x10000
	v_lshl_add_u64 v[234:235], v[250:251], 0, s[100:101]
	global_load_dwordx4 v[222:225], v[234:235], off offset:48
	global_load_dwordx4 v[226:229], v[234:235], off offset:32
	global_load_dwordx4 v[230:233], v[234:235], off offset:16
	s_nop 0
	global_load_dwordx4 v[234:237], v[234:235], off
	s_mov_b32 s100, 0x20000
	v_lshl_add_u64 v[192:193], v[250:251], 0, s[100:101]
	global_load_dwordx4 v[238:241], v[192:193], off offset:48
	global_load_dwordx4 v[242:245], v[192:193], off offset:32
	global_load_dwordx4 v[246:249], v[192:193], off offset:16
	s_nop 0
	global_load_dwordx4 v[192:195], v[192:193], off
	s_waitcnt vmcnt(12)
	v_pk_mul_f32 v[12:13], v[2:3], s[84:85] op_sel_hi:[1,0]
	v_pk_mul_f32 v[2:3], v[18:19], s[84:85] op_sel_hi:[1,0]
	v_lshl_add_u32 v18, s65, 8, v25
	v_ashrrev_i32_e32 v19, 31, v18
	v_pk_mul_f32 v[14:15], v[0:1], s[84:85] op_sel_hi:[1,0]
	v_pk_mul_f32 v[0:1], v[20:21], s[84:85] op_sel_hi:[1,0]
	v_lshlrev_b64 v[20:21], 10, v[18:19]
	v_lshl_add_u64 v[26:27], v[20:21], 0, v[16:17]
	v_pk_mul_f32 v[8:9], v[6:7], s[84:85] op_sel_hi:[1,0]
	v_pk_mul_f32 v[10:11], v[4:5], s[84:85] op_sel_hi:[1,0]
	v_pk_mul_f32 v[4:5], v[176:177], s[84:85] op_sel_hi:[1,0]
	v_pk_mul_f32 v[6:7], v[174:175], s[84:85] op_sel_hi:[1,0]
	v_lshl_add_u64 v[26:27], v[26:27], 1, s[50:51]
	s_waitcnt vmcnt(11)
	v_pk_mul_f32 v[22:23], v[208:209], s[86:87] op_sel_hi:[1,0]
	v_pk_mul_f32 v[20:21], v[206:207], s[86:87] op_sel_hi:[1,0]
	s_waitcnt vmcnt(9)
	v_pk_mul_f32 v[180:181], v[216:217], s[86:87] op_sel_hi:[1,0]
	v_pk_mul_f32 v[178:179], v[214:215], s[86:87] op_sel_hi:[1,0]
	s_waitcnt vmcnt(8)
	v_pk_mul_f32 v[182:183], v[220:221], s[86:87] op_sel_hi:[1,0]
	v_pk_mul_f32 v[188:189], v[218:219], s[86:87] op_sel_hi:[1,0]
	v_pk_fma_f32 v[180:181], v[146:147], v[8:9], v[180:181]
	v_pk_fma_f32 v[146:147], v[144:145], v[10:11], v[178:179]
	v_pk_fma_f32 v[154:155], v[154:155], v[12:13], v[182:183]
	v_pk_fma_f32 v[152:153], v[152:153], v[14:15], v[188:189]
	v_pk_fma_f32 v[150:151], v[150:151], v[0:1], v[22:23]
	v_cvt_pk_bf16_f32 v144, v152, v153
	v_cvt_pk_bf16_f32 v145, v154, v155
	v_cvt_pk_bf16_f32 v146, v146, v147
	v_cvt_pk_bf16_f32 v147, v180, v181
	ds_write_b128 v190, v[144:147]
	v_pk_fma_f32 v[22:23], v[148:149], v[2:3], v[20:21]
	s_nop 0
	v_pk_mul_f32 v[146:147], v[210:211], s[86:87] op_sel_hi:[1,0]
	v_pk_mul_f32 v[144:145], v[212:213], s[86:87] op_sel_hi:[1,0]
	v_pk_fma_f32 v[146:147], v[156:157], v[6:7], v[146:147]
	v_pk_fma_f32 v[144:145], v[158:159], v[4:5], v[144:145]
	v_cvt_pk_bf16_f32 v20, v146, v147
	s_nop 0
	v_cvt_pk_bf16_f32 v21, v144, v145
	v_cvt_pk_bf16_f32 v22, v22, v23
	v_cvt_pk_bf16_f32 v23, v150, v151
	ds_write_b128 v190, v[20:23] offset:16
	ds_read_b128 v[144:147], v191
	ds_read_b128 v[156:159], v191 offset:1152
	s_mov_b32 s100, 0x4000
	v_lshl_add_u64 v[188:189], v[26:27], 0, s[100:101]
	v_mov_b64_e32 v[178:179], v[26:27]
	s_nop 1
	v_or_b32_e32 v20, 16, v18
	v_ashrrev_i32_e32 v21, 31, v20
	v_lshlrev_b64 v[20:21], 10, v[20:21]
	v_lshl_add_u64 v[26:27], v[20:21], 0, v[16:17]
	s_mov_b32 s100, 0x30000
	v_lshl_add_u64 v[218:219], v[250:251], 0, s[100:101]
	global_load_dwordx4 v[206:209], v[218:219], off offset:48
	global_load_dwordx4 v[210:213], v[218:219], off offset:32
	global_load_dwordx4 v[214:217], v[218:219], off offset:16
	s_nop 0
	global_load_dwordx4 v[218:221], v[218:219], off
	v_lshl_add_u64 v[26:27], v[26:27], 1, s[50:51]
	s_waitcnt vmcnt(11)
	v_pk_mul_f32 v[22:23], v[224:225], s[86:87] op_sel_hi:[1,0]
	v_pk_mul_f32 v[20:21], v[222:223], s[86:87] op_sel_hi:[1,0]
	s_waitcnt vmcnt(9)
	v_pk_mul_f32 v[150:151], v[232:233], s[86:87] op_sel_hi:[1,0]
	v_pk_mul_f32 v[148:149], v[230:231], s[86:87] op_sel_hi:[1,0]
	s_waitcnt vmcnt(8)
; __device__ __forceinline__ unsigned cvt_pk_bf16(float lo, float hi) { unsigned r; asm volatile("v_cvt_pk_bf16_f32 %0, %1, %2" : "=v"(r) : "v"(lo), "v"(hi)); return r; }
;     __device__ __forceinline__ void operator()(const f32x4 (&acc)[2][2][4][2], const Unit& u, int wr, int wc, int fr, int fq, const LAS unsigned* rt) const {
;     ...
;         for (int ai = 0; ai < 2; ++ai)
; #pragma unroll
;             for (int m = 0; m < 4; ++m) { const size_t o = (size_t)(u.pm * BM + ai * HALF + wr * 64 + m * 16 + fr) * D + col0;
;                 const f32x4 x0 = *(const f32x4*)(x + o), x1 = *(const f32x4*)(x + o + 4), x2 = *(const f32x4*)(x + o + 8), x3 = *(const f32x4*)(x + o + 12);
;                 const f32x4 xs[2][2] = {{x0, x1}, {x2, x3}};
; #pragma unroll
;                 for (int bj = 0; bj < 2; ++bj) {
;                     const f32x4 t0 = xs[bj][0] * ALPHA + g[bj][0] * acc[ai][bj][m][0], t1 = xs[bj][1] * ALPHA + g[bj][1] * acc[ai][bj][m][1];
;                     u32x4 w; w.x = cvt_pk_bf16(t0[0], t0[1]); w.y = cvt_pk_bf16(t0[2], t0[3]); w.z = cvt_pk_bf16(t1[0], t1[1]); w.w = cvt_pk_bf16(t1[2], t1[3]);
;                     *(u32x4*)(tb + o + 8 * bj) = w; } }
	v_pk_mul_f32 v[154:155], v[236:237], s[86:87] op_sel_hi:[1,0]
	v_pk_mul_f32 v[152:153], v[234:235], s[86:87] op_sel_hi:[1,0]
	v_pk_fma_f32 v[150:151], v[130:131], v[8:9], v[150:151]
	v_pk_fma_f32 v[130:131], v[128:129], v[10:11], v[148:149]
	v_pk_fma_f32 v[138:139], v[138:139], v[12:13], v[154:155]
	v_pk_fma_f32 v[136:137], v[136:137], v[14:15], v[152:153]
	v_pk_fma_f32 v[134:135], v[134:135], v[0:1], v[22:23]
	v_cvt_pk_bf16_f32 v128, v136, v137
	v_cvt_pk_bf16_f32 v129, v138, v139
	v_cvt_pk_bf16_f32 v130, v130, v131
	v_cvt_pk_bf16_f32 v131, v150, v151
	s_waitcnt lgkmcnt(0)
	global_store_dwordx4 v[178:179], v[144:147], off
	global_store_dwordx4 v[188:189], v[156:159], off
	ds_write_b128 v190, v[128:131]
	v_pk_fma_f32 v[22:23], v[132:133], v[2:3], v[20:21]
	s_nop 0
	v_pk_mul_f32 v[130:131], v[226:227], s[86:87] op_sel_hi:[1,0]
	v_pk_mul_f32 v[128:129], v[228:229], s[86:87] op_sel_hi:[1,0]
	v_pk_fma_f32 v[130:131], v[140:141], v[6:7], v[130:131]
	v_pk_fma_f32 v[128:129], v[142:143], v[4:5], v[128:129]
	v_cvt_pk_bf16_f32 v20, v130, v131
	s_nop 0
	v_cvt_pk_bf16_f32 v21, v128, v129
	v_cvt_pk_bf16_f32 v22, v22, v23
	v_cvt_pk_bf16_f32 v23, v134, v135
	ds_write_b128 v190, v[20:23] offset:16
	ds_read_b128 v[128:131], v191
	ds_read_b128 v[140:143], v191 offset:1152
	s_mov_b32 s100, 0x4000
	v_lshl_add_u64 v[188:189], v[26:27], 0, s[100:101]
	v_mov_b64_e32 v[178:179], v[26:27]
	s_nop 1
	v_or_b32_e32 v20, 32, v18
	v_ashrrev_i32_e32 v21, 31, v20
	v_lshlrev_b64 v[20:21], 10, v[20:21]
	v_lshl_add_u64 v[26:27], v[20:21], 0, v[16:17]
	s_mov_b32 s100, 0x80000
	v_lshl_add_u64 v[234:235], v[250:251], 0, s[100:101]
	global_load_dwordx4 v[222:225], v[234:235], off offset:48
	global_load_dwordx4 v[226:229], v[234:235], off offset:32
	global_load_dwordx4 v[230:233], v[234:235], off offset:16
	s_nop 0
	global_load_dwordx4 v[234:237], v[234:235], off
	v_lshl_add_u64 v[26:27], v[26:27], 1, s[50:51]
	s_waitcnt vmcnt(13)
	v_pk_mul_f32 v[22:23], v[240:241], s[86:87] op_sel_hi:[1,0]
	v_pk_mul_f32 v[20:21], v[238:239], s[86:87] op_sel_hi:[1,0]
	s_waitcnt vmcnt(11)
	v_pk_mul_f32 v[134:135], v[248:249], s[86:87] op_sel_hi:[1,0]
	v_pk_mul_f32 v[132:133], v[246:247], s[86:87] op_sel_hi:[1,0]
	s_waitcnt vmcnt(10)
	v_pk_mul_f32 v[138:139], v[194:195], s[86:87] op_sel_hi:[1,0]
	v_pk_mul_f32 v[136:137], v[192:193], s[86:87] op_sel_hi:[1,0]
	v_pk_fma_f32 v[134:135], v[114:115], v[8:9], v[134:135]
	v_pk_fma_f32 v[114:115], v[112:113], v[10:11], v[132:133]
	v_pk_fma_f32 v[122:123], v[122:123], v[12:13], v[138:139]
	v_pk_fma_f32 v[120:121], v[120:121], v[14:15], v[136:137]
	v_pk_fma_f32 v[118:119], v[118:119], v[0:1], v[22:23]
	v_cvt_pk_bf16_f32 v112, v120, v121
	v_cvt_pk_bf16_f32 v113, v122, v123
	v_cvt_pk_bf16_f32 v114, v114, v115
	v_cvt_pk_bf16_f32 v115, v134, v135
	s_waitcnt lgkmcnt(0)
	global_store_dwordx4 v[178:179], v[128:131], off
	global_store_dwordx4 v[188:189], v[140:143], off
	ds_write_b128 v190, v[112:115]
	v_pk_fma_f32 v[22:23], v[116:117], v[2:3], v[20:21]
	s_nop 0
	v_pk_mul_f32 v[114:115], v[242:243], s[86:87] op_sel_hi:[1,0]
	v_pk_mul_f32 v[112:113], v[244:245], s[86:87] op_sel_hi:[1,0]
	v_pk_fma_f32 v[114:115], v[124:125], v[6:7], v[114:115]
	v_pk_fma_f32 v[112:113], v[126:127], v[4:5], v[112:113]
	v_cvt_pk_bf16_f32 v20, v114, v115
	s_nop 0
	v_cvt_pk_bf16_f32 v21, v112, v113
	v_cvt_pk_bf16_f32 v22, v22, v23
	v_cvt_pk_bf16_f32 v23, v118, v119
	ds_write_b128 v190, v[20:23] offset:16
	ds_read_b128 v[112:115], v191
	ds_read_b128 v[124:127], v191 offset:1152
	s_mov_b32 s100, 0x4000
	v_lshl_add_u64 v[188:189], v[26:27], 0, s[100:101]
	v_mov_b64_e32 v[178:179], v[26:27]
	s_nop 1
	v_or_b32_e32 v20, 48, v18
	v_ashrrev_i32_e32 v21, 31, v20
	v_lshlrev_b64 v[20:21], 10, v[20:21]
	v_lshl_add_u64 v[26:27], v[20:21], 0, v[16:17]
	s_mov_b32 s100, 0x90000
	v_lshl_add_u64 v[192:193], v[250:251], 0, s[100:101]
	global_load_dwordx4 v[238:241], v[192:193], off offset:48
	global_load_dwordx4 v[242:245], v[192:193], off offset:32
	global_load_dwordx4 v[246:249], v[192:193], off offset:16
	s_nop 0
	global_load_dwordx4 v[192:195], v[192:193], off
	v_lshl_add_u64 v[26:27], v[26:27], 1, s[50:51]
	s_waitcnt vmcnt(13)
	v_pk_mul_f32 v[22:23], v[208:209], s[86:87] op_sel_hi:[1,0]
	v_pk_mul_f32 v[20:21], v[206:207], s[86:87] op_sel_hi:[1,0]
	s_waitcnt vmcnt(11)
	v_pk_mul_f32 v[118:119], v[216:217], s[86:87] op_sel_hi:[1,0]
	v_pk_mul_f32 v[116:117], v[214:215], s[86:87] op_sel_hi:[1,0]
	s_waitcnt vmcnt(10)
	v_pk_mul_f32 v[122:123], v[220:221], s[86:87] op_sel_hi:[1,0]
	v_pk_mul_f32 v[120:121], v[218:219], s[86:87] op_sel_hi:[1,0]
	v_pk_fma_f32 v[118:119], v[98:99], v[8:9], v[118:119]
	v_pk_fma_f32 v[98:99], v[96:97], v[10:11], v[116:117]
	v_pk_fma_f32 v[106:107], v[106:107], v[12:13], v[122:123]
	v_pk_fma_f32 v[104:105], v[104:105], v[14:15], v[120:121]
	v_pk_fma_f32 v[102:103], v[102:103], v[0:1], v[22:23]
	v_cvt_pk_bf16_f32 v96, v104, v105
	v_cvt_pk_bf16_f32 v97, v106, v107
	v_cvt_pk_bf16_f32 v98, v98, v99
	v_cvt_pk_bf16_f32 v99, v118, v119
	s_waitcnt lgkmcnt(0)
; __device__ __forceinline__ unsigned cvt_pk_bf16(float lo, float hi) { unsigned r; asm volatile("v_cvt_pk_bf16_f32 %0, %1, %2" : "=v"(r) : "v"(lo), "v"(hi)); return r; }
;     __device__ __forceinline__ void operator()(const f32x4 (&acc)[2][2][4][2], const Unit& u, int wr, int wc, int fr, int fq, const LAS unsigned* rt) const {
;     ...
;         for (int ai = 0; ai < 2; ++ai)
; #pragma unroll
;             for (int m = 0; m < 4; ++m) { const size_t o = (size_t)(u.pm * BM + ai * HALF + wr * 64 + m * 16 + fr) * D + col0;
;                 const f32x4 x0 = *(const f32x4*)(x + o), x1 = *(const f32x4*)(x + o + 4), x2 = *(const f32x4*)(x + o + 8), x3 = *(const f32x4*)(x + o + 12);
;                 const f32x4 xs[2][2] = {{x0, x1}, {x2, x3}};
; #pragma unroll
;                 for (int bj = 0; bj < 2; ++bj) {
;                     const f32x4 t0 = xs[bj][0] * ALPHA + g[bj][0] * acc[ai][bj][m][0], t1 = xs[bj][1] * ALPHA + g[bj][1] * acc[ai][bj][m][1];
;                     u32x4 w; w.x = cvt_pk_bf16(t0[0], t0[1]); w.y = cvt_pk_bf16(t0[2], t0[3]); w.z = cvt_pk_bf16(t1[0], t1[1]); w.w = cvt_pk_bf16(t1[2], t1[3]);
;                     *(u32x4*)(tb + o + 8 * bj) = w; } }
	global_store_dwordx4 v[178:179], v[112:115], off
	global_store_dwordx4 v[188:189], v[124:127], off
	ds_write_b128 v190, v[96:99]
	v_pk_fma_f32 v[22:23], v[100:101], v[2:3], v[20:21]
	s_nop 0
	v_pk_mul_f32 v[98:99], v[210:211], s[86:87] op_sel_hi:[1,0]
	v_pk_mul_f32 v[96:97], v[212:213], s[86:87] op_sel_hi:[1,0]
	v_pk_fma_f32 v[98:99], v[108:109], v[6:7], v[98:99]
	v_pk_fma_f32 v[96:97], v[110:111], v[4:5], v[96:97]
	v_cvt_pk_bf16_f32 v20, v98, v99
	s_nop 0
	v_cvt_pk_bf16_f32 v21, v96, v97
	v_cvt_pk_bf16_f32 v22, v22, v23
	v_cvt_pk_bf16_f32 v23, v102, v103
	ds_write_b128 v190, v[20:23] offset:16
	ds_read_b128 v[96:99], v191
	ds_read_b128 v[108:111], v191 offset:1152
	s_mov_b32 s100, 0x4000
	v_lshl_add_u64 v[188:189], v[26:27], 0, s[100:101]
	v_mov_b64_e32 v[178:179], v[26:27]
	s_nop 1
	v_add_u32_e32 v20, 0x80, v18
	v_ashrrev_i32_e32 v21, 31, v20
	v_lshlrev_b64 v[20:21], 10, v[20:21]
	v_lshl_add_u64 v[26:27], v[20:21], 0, v[16:17]
	s_mov_b32 s100, 0xa0000
	v_lshl_add_u64 v[218:219], v[250:251], 0, s[100:101]
	global_load_dwordx4 v[206:209], v[218:219], off offset:48
	global_load_dwordx4 v[210:213], v[218:219], off offset:32
	global_load_dwordx4 v[214:217], v[218:219], off offset:16
	s_nop 0
	global_load_dwordx4 v[218:221], v[218:219], off
	v_lshl_add_u64 v[26:27], v[26:27], 1, s[50:51]
	s_waitcnt vmcnt(13)
	v_pk_mul_f32 v[22:23], v[224:225], s[86:87] op_sel_hi:[1,0]
	v_pk_mul_f32 v[20:21], v[222:223], s[86:87] op_sel_hi:[1,0]
	s_waitcnt vmcnt(11)
	v_pk_mul_f32 v[102:103], v[232:233], s[86:87] op_sel_hi:[1,0]
	v_pk_mul_f32 v[100:101], v[230:231], s[86:87] op_sel_hi:[1,0]
	s_waitcnt vmcnt(10)
	v_pk_mul_f32 v[106:107], v[236:237], s[86:87] op_sel_hi:[1,0]
	v_pk_mul_f32 v[104:105], v[234:235], s[86:87] op_sel_hi:[1,0]
	v_pk_fma_f32 v[102:103], v[82:83], v[8:9], v[102:103]
	v_pk_fma_f32 v[82:83], v[80:81], v[10:11], v[100:101]
	v_pk_fma_f32 v[90:91], v[90:91], v[12:13], v[106:107]
	v_pk_fma_f32 v[88:89], v[88:89], v[14:15], v[104:105]
	v_pk_fma_f32 v[86:87], v[86:87], v[0:1], v[22:23]
	v_cvt_pk_bf16_f32 v80, v88, v89
	v_cvt_pk_bf16_f32 v81, v90, v91
	v_cvt_pk_bf16_f32 v82, v82, v83
	v_cvt_pk_bf16_f32 v83, v102, v103
	s_waitcnt lgkmcnt(0)
	global_store_dwordx4 v[178:179], v[96:99], off
	global_store_dwordx4 v[188:189], v[108:111], off
	ds_write_b128 v190, v[80:83]
	v_pk_fma_f32 v[22:23], v[84:85], v[2:3], v[20:21]
	s_nop 0
	v_pk_mul_f32 v[82:83], v[226:227], s[86:87] op_sel_hi:[1,0]
	v_pk_mul_f32 v[80:81], v[228:229], s[86:87] op_sel_hi:[1,0]
	v_pk_fma_f32 v[82:83], v[92:93], v[6:7], v[82:83]
	v_pk_fma_f32 v[80:81], v[94:95], v[4:5], v[80:81]
	v_cvt_pk_bf16_f32 v20, v82, v83
	s_nop 0
	v_cvt_pk_bf16_f32 v21, v80, v81
	v_cvt_pk_bf16_f32 v22, v22, v23
	v_cvt_pk_bf16_f32 v23, v86, v87
	ds_write_b128 v190, v[20:23] offset:16
	ds_read_b128 v[80:83], v191
	ds_read_b128 v[92:95], v191 offset:1152
	s_mov_b32 s100, 0x4000
	v_lshl_add_u64 v[188:189], v[26:27], 0, s[100:101]
	v_mov_b64_e32 v[178:179], v[26:27]
	s_nop 1
	v_add_u32_e32 v20, 0x90, v18
	v_ashrrev_i32_e32 v21, 31, v20
	v_lshlrev_b64 v[20:21], 10, v[20:21]
	v_lshl_add_u64 v[26:27], v[20:21], 0, v[16:17]
	s_mov_b32 s100, 0xb0000
	v_lshl_add_u64 v[234:235], v[250:251], 0, s[100:101]
	global_load_dwordx4 v[222:225], v[234:235], off offset:48
	global_load_dwordx4 v[226:229], v[234:235], off offset:32
	global_load_dwordx4 v[230:233], v[234:235], off offset:16
	s_nop 0
	global_load_dwordx4 v[234:237], v[234:235], off
	v_lshl_add_u64 v[26:27], v[26:27], 1, s[50:51]
	s_waitcnt vmcnt(13)
	v_pk_mul_f32 v[22:23], v[240:241], s[86:87] op_sel_hi:[1,0]
	v_pk_mul_f32 v[20:21], v[238:239], s[86:87] op_sel_hi:[1,0]
	s_waitcnt vmcnt(11)
	v_pk_mul_f32 v[86:87], v[248:249], s[86:87] op_sel_hi:[1,0]
	v_pk_mul_f32 v[84:85], v[246:247], s[86:87] op_sel_hi:[1,0]
	s_waitcnt vmcnt(10)
	v_pk_mul_f32 v[90:91], v[194:195], s[86:87] op_sel_hi:[1,0]
	v_pk_mul_f32 v[88:89], v[192:193], s[86:87] op_sel_hi:[1,0]
	v_pk_fma_f32 v[86:87], v[66:67], v[8:9], v[86:87]
	v_pk_fma_f32 v[66:67], v[64:65], v[10:11], v[84:85]
	v_pk_fma_f32 v[74:75], v[74:75], v[12:13], v[90:91]
	v_pk_fma_f32 v[72:73], v[72:73], v[14:15], v[88:89]
	v_pk_fma_f32 v[70:71], v[70:71], v[0:1], v[22:23]
	v_cvt_pk_bf16_f32 v64, v72, v73
	v_cvt_pk_bf16_f32 v65, v74, v75
	v_cvt_pk_bf16_f32 v66, v66, v67
	v_cvt_pk_bf16_f32 v67, v86, v87
	s_waitcnt lgkmcnt(0)
; __device__ __forceinline__ unsigned cvt_pk_bf16(float lo, float hi) { unsigned r; asm volatile("v_cvt_pk_bf16_f32 %0, %1, %2" : "=v"(r) : "v"(lo), "v"(hi)); return r; }
;     __device__ __forceinline__ void operator()(const f32x4 (&acc)[2][2][4][2], const Unit& u, int wr, int wc, int fr, int fq, const LAS unsigned* rt) const {
;     ...
;         for (int ai = 0; ai < 2; ++ai)
; #pragma unroll
;             for (int m = 0; m < 4; ++m) { const size_t o = (size_t)(u.pm * BM + ai * HALF + wr * 64 + m * 16 + fr) * D + col0;
;                 const f32x4 x0 = *(const f32x4*)(x + o), x1 = *(const f32x4*)(x + o + 4), x2 = *(const f32x4*)(x + o + 8), x3 = *(const f32x4*)(x + o + 12);
;                 const f32x4 xs[2][2] = {{x0, x1}, {x2, x3}};
; #pragma unroll
;                 for (int bj = 0; bj < 2; ++bj) {
;                     const f32x4 t0 = xs[bj][0] * ALPHA + g[bj][0] * acc[ai][bj][m][0], t1 = xs[bj][1] * ALPHA + g[bj][1] * acc[ai][bj][m][1];
;                     u32x4 w; w.x = cvt_pk_bf16(t0[0], t0[1]); w.y = cvt_pk_bf16(t0[2], t0[3]); w.z = cvt_pk_bf16(t1[0], t1[1]); w.w = cvt_pk_bf16(t1[2], t1[3]);
;                     *(u32x4*)(tb + o + 8 * bj) = w; } }
	global_store_dwordx4 v[178:179], v[80:83], off
	global_store_dwordx4 v[188:189], v[92:95], off
	ds_write_b128 v190, v[64:67]
	v_pk_fma_f32 v[22:23], v[68:69], v[2:3], v[20:21]
	s_nop 0
	v_pk_mul_f32 v[66:67], v[242:243], s[86:87] op_sel_hi:[1,0]
	v_pk_mul_f32 v[64:65], v[244:245], s[86:87] op_sel_hi:[1,0]
	v_pk_fma_f32 v[66:67], v[76:77], v[6:7], v[66:67]
	v_pk_fma_f32 v[64:65], v[78:79], v[4:5], v[64:65]
	v_cvt_pk_bf16_f32 v20, v66, v67
	s_nop 0
	v_cvt_pk_bf16_f32 v21, v64, v65
	v_cvt_pk_bf16_f32 v22, v22, v23
	v_cvt_pk_bf16_f32 v23, v70, v71
	ds_write_b128 v190, v[20:23] offset:16
	ds_read_b128 v[64:67], v191
	ds_read_b128 v[76:79], v191 offset:1152
	s_mov_b32 s100, 0x4000
	v_lshl_add_u64 v[188:189], v[26:27], 0, s[100:101]
	v_mov_b64_e32 v[178:179], v[26:27]
	s_nop 1
	v_add_u32_e32 v20, 0xa0, v18
	v_ashrrev_i32_e32 v21, 31, v20
	v_lshlrev_b64 v[20:21], 10, v[20:21]
	v_lshl_add_u64 v[26:27], v[20:21], 0, v[16:17]
	v_add_u32_e32 v18, 0xb0, v18
	v_lshl_add_u64 v[26:27], v[26:27], 1, s[50:51]
	v_ashrrev_i32_e32 v19, 31, v18
	v_lshlrev_b64 v[18:19], 10, v[18:19]
	s_waitcnt vmcnt(9)
	v_pk_mul_f32 v[22:23], v[208:209], s[86:87] op_sel_hi:[1,0]
	v_pk_mul_f32 v[20:21], v[206:207], s[86:87] op_sel_hi:[1,0]
	s_waitcnt vmcnt(7)
	v_pk_mul_f32 v[70:71], v[216:217], s[86:87] op_sel_hi:[1,0]
	v_pk_mul_f32 v[68:69], v[214:215], s[86:87] op_sel_hi:[1,0]
	s_waitcnt vmcnt(6)
	v_pk_mul_f32 v[74:75], v[220:221], s[86:87] op_sel_hi:[1,0]
	v_pk_mul_f32 v[72:73], v[218:219], s[86:87] op_sel_hi:[1,0]
	v_pk_fma_f32 v[70:71], v[50:51], v[8:9], v[70:71]
	v_pk_fma_f32 v[50:51], v[48:49], v[10:11], v[68:69]
	v_pk_fma_f32 v[58:59], v[58:59], v[12:13], v[74:75]
	v_pk_fma_f32 v[56:57], v[56:57], v[14:15], v[72:73]
	v_pk_fma_f32 v[54:55], v[54:55], v[0:1], v[22:23]
	v_cvt_pk_bf16_f32 v48, v56, v57
	v_cvt_pk_bf16_f32 v49, v58, v59
	v_cvt_pk_bf16_f32 v50, v50, v51
	v_cvt_pk_bf16_f32 v51, v70, v71
	s_waitcnt lgkmcnt(0)
	global_store_dwordx4 v[178:179], v[64:67], off
	global_store_dwordx4 v[188:189], v[76:79], off
	ds_write_b128 v190, v[48:51]
	v_pk_fma_f32 v[22:23], v[52:53], v[2:3], v[20:21]
	s_nop 0
	v_pk_mul_f32 v[48:49], v[212:213], s[86:87] op_sel_hi:[1,0]
	v_pk_mul_f32 v[50:51], v[210:211], s[86:87] op_sel_hi:[1,0]
	v_pk_fma_f32 v[48:49], v[62:63], v[4:5], v[48:49]
	v_pk_fma_f32 v[50:51], v[60:61], v[6:7], v[50:51]
	s_nop 0
	v_cvt_pk_bf16_f32 v20, v50, v51
	v_cvt_pk_bf16_f32 v21, v48, v49
	v_cvt_pk_bf16_f32 v22, v22, v23
	v_cvt_pk_bf16_f32 v23, v54, v55
	ds_write_b128 v190, v[20:23] offset:16
	ds_read_b128 v[48:51], v191
	ds_read_b128 v[60:63], v191 offset:1152
	s_mov_b32 s100, 0x4000
	v_lshl_add_u64 v[188:189], v[26:27], 0, s[100:101]
	v_mov_b64_e32 v[178:179], v[26:27]
	v_lshl_add_u64 v[26:27], v[18:19], 0, v[16:17]
	s_waitcnt vmcnt(2)
	v_pk_mul_f32 v[54:55], v[236:237], s[86:87] op_sel_hi:[1,0]
	v_pk_mul_f32 v[52:53], v[234:235], s[86:87] op_sel_hi:[1,0]
	v_pk_fma_f32 v[12:13], v[46:47], v[12:13], v[54:55]
	v_pk_mul_f32 v[46:47], v[230:231], s[86:87] op_sel_hi:[1,0]
	v_pk_fma_f32 v[14:15], v[44:45], v[14:15], v[52:53]
	v_pk_mul_f32 v[44:45], v[232:233], s[86:87] op_sel_hi:[1,0]
	v_pk_fma_f32 v[10:11], v[40:41], v[10:11], v[46:47]
	v_pk_fma_f32 v[42:43], v[42:43], v[8:9], v[44:45]
	v_cvt_pk_bf16_f32 v8, v14, v15
	v_cvt_pk_bf16_f32 v9, v12, v13
	v_cvt_pk_bf16_f32 v10, v10, v11
	v_lshl_add_u64 v[12:13], v[26:27], 1, s[50:51]
	v_cvt_pk_bf16_f32 v11, v42, v43
	s_waitcnt lgkmcnt(0)
	global_store_dwordx4 v[178:179], v[48:51], off
	global_store_dwordx4 v[188:189], v[60:63], off
	ds_write_b128 v190, v[8:11]
	s_nop 1
	v_pk_mul_f32 v[10:11], v[226:227], s[86:87] op_sel_hi:[1,0]
	v_pk_mul_f32 v[8:9], v[228:229], s[86:87] op_sel_hi:[1,0]
	v_pk_fma_f32 v[6:7], v[36:37], v[6:7], v[10:11]
	v_pk_mul_f32 v[10:11], v[222:223], s[86:87] op_sel_hi:[1,0]
	v_pk_fma_f32 v[4:5], v[38:39], v[4:5], v[8:9]
	v_pk_mul_f32 v[8:9], v[224:225], s[86:87] op_sel_hi:[1,0]
	v_pk_fma_f32 v[2:3], v[32:33], v[2:3], v[10:11]
	v_pk_fma_f32 v[8:9], v[34:35], v[0:1], v[8:9]
	v_cvt_pk_bf16_f32 v0, v6, v7
	v_cvt_pk_bf16_f32 v1, v4, v5
	v_cvt_pk_bf16_f32 v2, v2, v3
	s_nop 0
	v_cvt_pk_bf16_f32 v3, v8, v9
	ds_write_b128 v190, v[0:3] offset:16
	ds_read_b128 v[8:11], v191
	ds_read_b128 v[0:3], v191 offset:1152
	s_mov_b32 s100, 0x4000
	v_lshl_add_u64 v[188:189], v[12:13], 0, s[100:101]
	s_waitcnt lgkmcnt(0)
	global_store_dwordx4 v[12:13], v[8:11], off
	global_store_dwordx4 v[188:189], v[0:3], off
	s_cbranch_scc1 .LBB0_404
	s_and_b64 s[4:5], s[8:9], exec
	s_cselect_b32 s12, s64, s12
	s_andn2_b64 vcc, exec, s[10:11]
	s_cbranch_vccnz .LBB0_403
	s_barrier
	s_branch .LBB0_403
